# adds GEMM accumulator clearing with 64-bit moves (64 instead of 127 instructions per unit)
# speedup vs baseline: 1.0160x; 1.0160x over previous
; #define PG8_SETVO(dst, u) do { _Pragma("unroll") for (int _h = 0; _h < 2; ++_h) _Pragma("unroll") for (int _i = 0; _i < 2; ++_i) { \
;         if constexpr (GATHER) { int R_, C_; stage_rc(tid * 16 + _i * 8192, R_, C_); dst[_h][_i] = (unsigned)(S.arow(u, R_ + HALF * _h) * K + C_) * 2u; } \
;         else dst[_h][_i] = voffA[_i] + (unsigned)_h * (unsigned)(HALF * K * 2); } } while (0)
; template <class Epi, class Sched, bool ALIGN_EPI = false, bool SP2 = false, bool F8 = false, bool GATHER = false>
; __device__ __forceinline__ void gemm_phase(PG8_LAS unsigned char* lds, const Gemm g, const Sched& S, const Epi& E) {
;     ...
;         const char* nA = (has_next && !GATHER) ? (const char*)g.A + (size_t)nxt.pm * tstep : cA; const char* nB = has_next ? (const char*)g.Bt + (size_t)nxt.pn * tstep : cB;
;         if (has_next) { PG8_SETVO(nvo, nxt); } else {
; #pragma unroll
;             for (int _h = 0; _h < 2; ++_h)
; #pragma unroll
;                 for (int _i = 0; _i < 2; ++_i) nvo[_h][_i] = vo[_h][_i]; }
;         for (int t = 0; t < nt; t += 2) {
;             const bool last = (t == nt - 2);
;             const char* a1 = cA + (size_t)(t + 1) * kstep;
;             const char* a2 = last ? nA : cA + (size_t)(t + 2) * kstep; const char* b2 = last ? nB : cB + (size_t)(t + 2) * kstep;
;             const char* a3 = a2 + kstep; const char* b3 = b2 + kstep;
;     ...
; #pragma unroll
;         for (int a = 0; a < 2; ++a)
; #pragma unroll
;             for (int b = 0; b < 2; ++b)
; #pragma unroll
;                 for (int m = 0; m < 4; ++m)
; #pragma unroll
;                     for (int n = 0; n < 2; ++n) acc[a][b][m][n] = (f32x4){0.f, 0.f, 0.f, 0.f};
.LBB0_122:
	s_ashr_i32 s75, s74, 31
	s_lshl_b64 s[52:53], s[74:75], 19
	s_add_u32 s76, s0, s52
	s_addc_u32 s77, s1, s53
	s_and_b64 s[52:53], s[8:9], exec
	s_cselect_b32 s5, s77, s81
	s_cselect_b32 s7, s76, s80
	s_ashr_i32 s73, s72, 31
	s_lshl_b64 s[52:53], s[72:73], 19
	s_add_u32 s78, s2, s52
	s_addc_u32 s79, s3, s53
	s_and_b64 s[52:53], s[8:9], exec
	s_cselect_b32 s44, s79, s83
	s_cselect_b32 s51, s78, s82
	s_add_u32 s80, s80, 0x80
	s_addc_u32 s81, s81, 0
	s_add_u32 s52, s82, 0x100
	v_mov_b32_e32 v34, 0
	s_addc_u32 s53, s83, 0
	s_mov_b32 s64, -2
	v_mov_b32_e32 v35, v34
	v_mov_b64_e32 v[36:37], v[34:35]
	v_mov_b64_e32 v[38:39], v[34:35]
	v_mov_b64_e32 v[40:41], v[34:35]
	v_mov_b64_e32 v[42:43], v[34:35]
	v_mov_b64_e32 v[44:45], v[34:35]
	v_mov_b64_e32 v[46:47], v[34:35]
	v_mov_b64_e32 v[48:49], v[34:35]
	v_mov_b64_e32 v[50:51], v[34:35]
	v_mov_b64_e32 v[52:53], v[34:35]
	v_mov_b64_e32 v[54:55], v[34:35]
	v_mov_b64_e32 v[56:57], v[34:35]
	v_mov_b64_e32 v[58:59], v[34:35]
	v_mov_b64_e32 v[60:61], v[34:35]
	v_mov_b64_e32 v[62:63], v[34:35]
	v_mov_b64_e32 v[64:65], v[34:35]
	v_mov_b64_e32 v[66:67], v[34:35]
	v_mov_b64_e32 v[68:69], v[34:35]
	v_mov_b64_e32 v[70:71], v[34:35]
	v_mov_b64_e32 v[72:73], v[34:35]
	v_mov_b64_e32 v[74:75], v[34:35]
	v_mov_b64_e32 v[76:77], v[34:35]
	v_mov_b64_e32 v[78:79], v[34:35]
	v_mov_b64_e32 v[80:81], v[34:35]
	v_mov_b64_e32 v[82:83], v[34:35]
	v_mov_b64_e32 v[84:85], v[34:35]
	v_mov_b64_e32 v[86:87], v[34:35]
	v_mov_b64_e32 v[88:89], v[34:35]
	v_mov_b64_e32 v[90:91], v[34:35]
	v_mov_b64_e32 v[92:93], v[34:35]
	v_mov_b64_e32 v[94:95], v[34:35]
	v_mov_b64_e32 v[96:97], v[34:35]
	v_mov_b64_e32 v[98:99], v[34:35]
	v_mov_b64_e32 v[100:101], v[34:35]
	v_mov_b64_e32 v[102:103], v[34:35]
	v_mov_b64_e32 v[104:105], v[34:35]
	v_mov_b64_e32 v[106:107], v[34:35]
	v_mov_b64_e32 v[108:109], v[34:35]
	v_mov_b64_e32 v[110:111], v[34:35]
	v_mov_b64_e32 v[112:113], v[34:35]
	v_mov_b64_e32 v[114:115], v[34:35]
	v_mov_b64_e32 v[116:117], v[34:35]
	v_mov_b64_e32 v[118:119], v[34:35]
	v_mov_b64_e32 v[120:121], v[34:35]
	v_mov_b64_e32 v[122:123], v[34:35]
	v_mov_b64_e32 v[124:125], v[34:35]
	v_mov_b64_e32 v[126:127], v[34:35]
	v_mov_b64_e32 v[128:129], v[34:35]
	v_mov_b64_e32 v[130:131], v[34:35]
	v_mov_b64_e32 v[132:133], v[34:35]
	v_mov_b64_e32 v[134:135], v[34:35]
	v_mov_b64_e32 v[136:137], v[34:35]
	v_mov_b64_e32 v[138:139], v[34:35]
	v_mov_b64_e32 v[140:141], v[34:35]
	v_mov_b64_e32 v[142:143], v[34:35]
	v_mov_b64_e32 v[144:145], v[34:35]
	v_mov_b64_e32 v[146:147], v[34:35]
	v_mov_b64_e32 v[148:149], v[34:35]
	v_mov_b64_e32 v[150:151], v[34:35]
	v_mov_b64_e32 v[152:153], v[34:35]
	v_mov_b64_e32 v[154:155], v[34:35]
	v_mov_b64_e32 v[156:157], v[34:35]
	v_mov_b64_e32 v[158:159], v[34:35]
	v_mov_b64_e32 v[160:161], v[34:35]

; #define PG8_SETVO(dst, u) do { _Pragma("unroll") for (int _h = 0; _h < 2; ++_h) _Pragma("unroll") for (int _i = 0; _i < 2; ++_i) { \
;         if constexpr (GATHER) { int R_, C_; stage_rc(tid * 16 + _i * 8192, R_, C_); dst[_h][_i] = (unsigned)(S.arow(u, R_ + HALF * _h) * K + C_) * 2u; } \
;         else dst[_h][_i] = voffA[_i] + (unsigned)_h * (unsigned)(HALF * K * 2); } } while (0)
; template <class Epi, class Sched, bool ALIGN_EPI = false, bool SP2 = false, bool F8 = false, bool GATHER = false>
; __device__ __forceinline__ void gemm_phase(PG8_LAS unsigned char* lds, const Gemm g, const Sched& S, const Epi& E) {
;     ...
;         const char* nA = (has_next && !GATHER) ? (const char*)g.A + (size_t)nxt.pm * tstep : cA; const char* nB = has_next ? (const char*)g.Bt + (size_t)nxt.pn * tstep : cB;
;         if (has_next) { PG8_SETVO(nvo, nxt); } else {
; #pragma unroll
;             for (int _h = 0; _h < 2; ++_h)
; #pragma unroll
;                 for (int _i = 0; _i < 2; ++_i) nvo[_h][_i] = vo[_h][_i]; }
;         for (int t = 0; t < nt; t += 2) {
;             const bool last = (t == nt - 2);
;             const char* a1 = cA + (size_t)(t + 1) * kstep;
;             const char* a2 = last ? nA : cA + (size_t)(t + 2) * kstep; const char* b2 = last ? nB : cB + (size_t)(t + 2) * kstep;
;             const char* a3 = a2 + kstep; const char* b3 = b2 + kstep;
;     ...
; #pragma unroll
;         for (int a = 0; a < 2; ++a)
; #pragma unroll
;             for (int b = 0; b < 2; ++b)
; #pragma unroll
;                 for (int m = 0; m < 4; ++m)
; #pragma unroll
;                     for (int n = 0; n < 2; ++n) acc[a][b][m][n] = (f32x4){0.f, 0.f, 0.f, 0.f};
.LBB0_729:
	s_ashr_i32 s47, s46, 31
	s_lshl_b64 s[54:55], s[46:47], 18
	s_add_u32 s54, s2, s54
	s_addc_u32 s55, s3, s55
	s_and_b64 s[56:57], s[4:5], exec
	s_cselect_b32 s47, s55, s61
	s_cselect_b32 s70, s54, s60
	s_ashr_i32 s45, s44, 31
	s_lshl_b64 s[56:57], s[44:45], 18
	s_add_u32 s56, s10, s56
	s_addc_u32 s57, s11, s57
	s_and_b64 s[64:65], s[4:5], exec
	s_cselect_b32 s45, s57, s63
	s_cselect_b32 s71, s56, s62
	s_add_u32 s60, s60, 0x80
	s_addc_u32 s61, s61, 0
	s_add_u32 s72, s62, 0x100
	v_mov_b32_e32 v34, 0
	s_addc_u32 s73, s63, 0
	s_mov_b32 s74, -2
	v_mov_b32_e32 v35, v34
	v_mov_b64_e32 v[36:37], v[34:35]
	v_mov_b64_e32 v[38:39], v[34:35]
	v_mov_b64_e32 v[40:41], v[34:35]
	v_mov_b64_e32 v[42:43], v[34:35]
	v_mov_b64_e32 v[44:45], v[34:35]
	v_mov_b64_e32 v[46:47], v[34:35]
	v_mov_b64_e32 v[48:49], v[34:35]
	v_mov_b64_e32 v[50:51], v[34:35]
	v_mov_b64_e32 v[52:53], v[34:35]
	v_mov_b64_e32 v[54:55], v[34:35]
	v_mov_b64_e32 v[56:57], v[34:35]
	v_mov_b64_e32 v[58:59], v[34:35]
	v_mov_b64_e32 v[60:61], v[34:35]
	v_mov_b64_e32 v[62:63], v[34:35]
	v_mov_b64_e32 v[64:65], v[34:35]
	v_mov_b64_e32 v[66:67], v[34:35]
	v_mov_b64_e32 v[68:69], v[34:35]
	v_mov_b64_e32 v[70:71], v[34:35]
	v_mov_b64_e32 v[72:73], v[34:35]
	v_mov_b64_e32 v[74:75], v[34:35]
	v_mov_b64_e32 v[76:77], v[34:35]
	v_mov_b64_e32 v[78:79], v[34:35]
	v_mov_b64_e32 v[80:81], v[34:35]
	v_mov_b64_e32 v[82:83], v[34:35]
	v_mov_b64_e32 v[84:85], v[34:35]
	v_mov_b64_e32 v[86:87], v[34:35]
	v_mov_b64_e32 v[88:89], v[34:35]
	v_mov_b64_e32 v[90:91], v[34:35]
	v_mov_b64_e32 v[92:93], v[34:35]
	v_mov_b64_e32 v[94:95], v[34:35]
	v_mov_b64_e32 v[96:97], v[34:35]
	v_mov_b64_e32 v[98:99], v[34:35]
	v_mov_b64_e32 v[100:101], v[34:35]
	v_mov_b64_e32 v[102:103], v[34:35]
	v_mov_b64_e32 v[104:105], v[34:35]
	v_mov_b64_e32 v[106:107], v[34:35]
	v_mov_b64_e32 v[108:109], v[34:35]
	v_mov_b64_e32 v[110:111], v[34:35]
	v_mov_b64_e32 v[112:113], v[34:35]
	v_mov_b64_e32 v[114:115], v[34:35]
	v_mov_b64_e32 v[116:117], v[34:35]
	v_mov_b64_e32 v[118:119], v[34:35]
	v_mov_b64_e32 v[120:121], v[34:35]
	v_mov_b64_e32 v[122:123], v[34:35]
	v_mov_b64_e32 v[124:125], v[34:35]
	v_mov_b64_e32 v[126:127], v[34:35]
	v_mov_b64_e32 v[128:129], v[34:35]
	v_mov_b64_e32 v[130:131], v[34:35]
	v_mov_b64_e32 v[132:133], v[34:35]
	v_mov_b64_e32 v[134:135], v[34:35]
	v_mov_b64_e32 v[136:137], v[34:35]
	v_mov_b64_e32 v[138:139], v[34:35]
	v_mov_b64_e32 v[140:141], v[34:35]
	v_mov_b64_e32 v[142:143], v[34:35]
	v_mov_b64_e32 v[144:145], v[34:35]
	v_mov_b64_e32 v[146:147], v[34:35]
	v_mov_b64_e32 v[148:149], v[34:35]
	v_mov_b64_e32 v[150:151], v[34:35]
	v_mov_b64_e32 v[152:153], v[34:35]
	v_mov_b64_e32 v[154:155], v[34:35]
	v_mov_b64_e32 v[156:157], v[34:35]
	v_mov_b64_e32 v[158:159], v[34:35]
	v_mov_b64_e32 v[160:161], v[34:35]

; #define PG8_SETVO(dst, u) do { _Pragma("unroll") for (int _h = 0; _h < 2; ++_h) _Pragma("unroll") for (int _i = 0; _i < 2; ++_i) { \
;         if constexpr (GATHER) { int R_, C_; stage_rc(tid * 16 + _i * 8192, R_, C_); dst[_h][_i] = (unsigned)(S.arow(u, R_ + HALF * _h) * K + C_) * 2u; } \
;         else dst[_h][_i] = voffA[_i] + (unsigned)_h * (unsigned)(HALF * K * 2); } } while (0)
; template <class Epi, class Sched, bool ALIGN_EPI = false, bool SP2 = false, bool F8 = false, bool GATHER = false>
; __device__ __forceinline__ void gemm_phase(PG8_LAS unsigned char* lds, const Gemm g, const Sched& S, const Epi& E) {
;     ...
;         const char* nA = (has_next && !GATHER) ? (const char*)g.A + (size_t)nxt.pm * tstep : cA; const char* nB = has_next ? (const char*)g.Bt + (size_t)nxt.pn * tstep : cB;
;         if (has_next) { PG8_SETVO(nvo, nxt); } else {
; #pragma unroll
;             for (int _h = 0; _h < 2; ++_h)
; #pragma unroll
;                 for (int _i = 0; _i < 2; ++_i) nvo[_h][_i] = vo[_h][_i]; }
;         for (int t = 0; t < nt; t += 2) {
;             const bool last = (t == nt - 2);
;             const char* a1 = cA + (size_t)(t + 1) * kstep;
;             const char* a2 = last ? nA : cA + (size_t)(t + 2) * kstep; const char* b2 = last ? nB : cB + (size_t)(t + 2) * kstep;
;             const char* a3 = a2 + kstep; const char* b3 = b2 + kstep;
;     ...
; #pragma unroll
;         for (int a = 0; a < 2; ++a)
; #pragma unroll
;             for (int b = 0; b < 2; ++b)
; #pragma unroll
;                 for (int m = 0; m < 4; ++m)
; #pragma unroll
;                     for (int n = 0; n < 2; ++n) acc[a][b][m][n] = (f32x4){0.f, 0.f, 0.f, 0.f};
.LBB0_749:
	s_ashr_i32 s45, s44, 31
	s_lshl_b64 s[46:47], s[44:45], 18
	s_add_u32 s46, s3, s46
	s_addc_u32 s47, s10, s47
	s_and_b64 s[54:55], s[4:5], exec
	s_cselect_b32 s45, s47, s59
	s_cselect_b32 s65, s46, s58
	s_ashr_i32 s43, s42, 31
	s_lshl_b64 s[54:55], s[42:43], 18
	s_add_u32 s54, s11, s54
	s_addc_u32 s55, s33, s55
	s_and_b64 s[62:63], s[4:5], exec
	s_cselect_b32 s43, s55, s61
	s_cselect_b32 s66, s54, s60
	s_add_u32 s58, s58, 0x80
	s_addc_u32 s59, s59, 0
	s_add_u32 s67, s60, 0x100
	v_mov_b32_e32 v34, 0
	s_addc_u32 s68, s61, 0
	s_mov_b32 s69, -2
	v_mov_b32_e32 v35, v34
	v_mov_b64_e32 v[36:37], v[34:35]
	v_mov_b64_e32 v[38:39], v[34:35]
	v_mov_b64_e32 v[40:41], v[34:35]
	v_mov_b64_e32 v[42:43], v[34:35]
	v_mov_b64_e32 v[44:45], v[34:35]
	v_mov_b64_e32 v[46:47], v[34:35]
	v_mov_b64_e32 v[48:49], v[34:35]
	v_mov_b64_e32 v[50:51], v[34:35]
	v_mov_b64_e32 v[52:53], v[34:35]
	v_mov_b64_e32 v[54:55], v[34:35]
	v_mov_b64_e32 v[56:57], v[34:35]
	v_mov_b64_e32 v[58:59], v[34:35]
	v_mov_b64_e32 v[60:61], v[34:35]
	v_mov_b64_e32 v[62:63], v[34:35]
	v_mov_b64_e32 v[64:65], v[34:35]
	v_mov_b64_e32 v[66:67], v[34:35]
	v_mov_b64_e32 v[68:69], v[34:35]
	v_mov_b64_e32 v[70:71], v[34:35]
	v_mov_b64_e32 v[72:73], v[34:35]
	v_mov_b64_e32 v[74:75], v[34:35]
	v_mov_b64_e32 v[76:77], v[34:35]
	v_mov_b64_e32 v[78:79], v[34:35]
	v_mov_b64_e32 v[80:81], v[34:35]
	v_mov_b64_e32 v[82:83], v[34:35]
	v_mov_b64_e32 v[84:85], v[34:35]
	v_mov_b64_e32 v[86:87], v[34:35]
	v_mov_b64_e32 v[88:89], v[34:35]
	v_mov_b64_e32 v[90:91], v[34:35]
	v_mov_b64_e32 v[92:93], v[34:35]
	v_mov_b64_e32 v[94:95], v[34:35]
	v_mov_b64_e32 v[96:97], v[34:35]
	v_mov_b64_e32 v[98:99], v[34:35]
	v_mov_b64_e32 v[100:101], v[34:35]
	v_mov_b64_e32 v[102:103], v[34:35]
	v_mov_b64_e32 v[104:105], v[34:35]
	v_mov_b64_e32 v[106:107], v[34:35]
	v_mov_b64_e32 v[108:109], v[34:35]
	v_mov_b64_e32 v[110:111], v[34:35]
	v_mov_b64_e32 v[112:113], v[34:35]
	v_mov_b64_e32 v[114:115], v[34:35]
	v_mov_b64_e32 v[116:117], v[34:35]
	v_mov_b64_e32 v[118:119], v[34:35]
	v_mov_b64_e32 v[120:121], v[34:35]
	v_mov_b64_e32 v[122:123], v[34:35]
	v_mov_b64_e32 v[124:125], v[34:35]
	v_mov_b64_e32 v[126:127], v[34:35]
	v_mov_b64_e32 v[128:129], v[34:35]
	v_mov_b64_e32 v[130:131], v[34:35]
	v_mov_b64_e32 v[132:133], v[34:35]
	v_mov_b64_e32 v[134:135], v[34:35]
	v_mov_b64_e32 v[136:137], v[34:35]
	v_mov_b64_e32 v[138:139], v[34:35]
	v_mov_b64_e32 v[140:141], v[34:35]
	v_mov_b64_e32 v[142:143], v[34:35]
	v_mov_b64_e32 v[144:145], v[34:35]
	v_mov_b64_e32 v[146:147], v[34:35]
	v_mov_b64_e32 v[148:149], v[34:35]
	v_mov_b64_e32 v[150:151], v[34:35]
	v_mov_b64_e32 v[152:153], v[34:35]
	v_mov_b64_e32 v[154:155], v[34:35]
	v_mov_b64_e32 v[156:157], v[34:35]
	v_mov_b64_e32 v[158:159], v[34:35]
	v_mov_b64_e32 v[160:161], v[34:35]

; #define PG8_SETVO(dst, u) do { _Pragma("unroll") for (int _h = 0; _h < 2; ++_h) _Pragma("unroll") for (int _i = 0; _i < 2; ++_i) { \
;         if constexpr (GATHER) { int R_, C_; stage_rc(tid * 16 + _i * 8192, R_, C_); dst[_h][_i] = (unsigned)(S.arow(u, R_ + HALF * _h) * K + C_) * 2u; } \
;         else dst[_h][_i] = voffA[_i] + (unsigned)_h * (unsigned)(HALF * K * 2); } } while (0)
; template <class Epi, class Sched, bool ALIGN_EPI = false, bool SP2 = false, bool F8 = false, bool GATHER = false>
; __device__ __forceinline__ void gemm_phase(PG8_LAS unsigned char* lds, const Gemm g, const Sched& S, const Epi& E) {
;     ...
;         const char* nA = (has_next && !GATHER) ? (const char*)g.A + (size_t)nxt.pm * tstep : cA; const char* nB = has_next ? (const char*)g.Bt + (size_t)nxt.pn * tstep : cB;
;         if (has_next) { PG8_SETVO(nvo, nxt); } else {
; #pragma unroll
;             for (int _h = 0; _h < 2; ++_h)
; #pragma unroll
;                 for (int _i = 0; _i < 2; ++_i) nvo[_h][_i] = vo[_h][_i]; }
;         for (int t = 0; t < nt; t += 2) {
;             const bool last = (t == nt - 2);
;             const char* a1 = cA + (size_t)(t + 1) * kstep;
;             const char* a2 = last ? nA : cA + (size_t)(t + 2) * kstep; const char* b2 = last ? nB : cB + (size_t)(t + 2) * kstep;
;             const char* a3 = a2 + kstep; const char* b3 = b2 + kstep;
;     ...
; #pragma unroll
;         for (int a = 0; a < 2; ++a)
; #pragma unroll
;             for (int b = 0; b < 2; ++b)
; #pragma unroll
;                 for (int m = 0; m < 4; ++m)
; #pragma unroll
;                     for (int n = 0; n < 2; ++n) acc[a][b][m][n] = (f32x4){0.f, 0.f, 0.f, 0.f};
.LBB0_824:
	s_ashr_i32 s55, s54, 31
	s_lshl_b64 s[56:57], s[54:55], 19
	s_add_u32 s56, s0, s56
	s_addc_u32 s57, s1, s57
	s_and_b64 s[58:59], s[4:5], exec
	s_cselect_b32 s55, s57, s63
	s_cselect_b32 s70, s56, s62
	s_ashr_i32 s47, s46, 31
	s_lshl_b64 s[58:59], s[46:47], 19
	s_add_u32 s58, s2, s58
	s_addc_u32 s59, s3, s59
	s_and_b64 s[66:67], s[4:5], exec
	s_cselect_b32 s47, s59, s65
	s_cselect_b32 s71, s58, s64
	s_add_u32 s62, s62, 0x80
	s_addc_u32 s63, s63, 0
	s_add_u32 s72, s64, 0x100
	v_mov_b32_e32 v34, 0
	s_addc_u32 s73, s65, 0
	s_mov_b32 s74, -2
	v_mov_b32_e32 v35, v34
	v_mov_b64_e32 v[36:37], v[34:35]
	v_mov_b64_e32 v[38:39], v[34:35]
	v_mov_b64_e32 v[40:41], v[34:35]
	v_mov_b64_e32 v[42:43], v[34:35]
	v_mov_b64_e32 v[44:45], v[34:35]
	v_mov_b64_e32 v[46:47], v[34:35]
	v_mov_b64_e32 v[48:49], v[34:35]
	v_mov_b64_e32 v[50:51], v[34:35]
	v_mov_b64_e32 v[52:53], v[34:35]
	v_mov_b64_e32 v[54:55], v[34:35]
	v_mov_b64_e32 v[56:57], v[34:35]
	v_mov_b64_e32 v[58:59], v[34:35]
	v_mov_b64_e32 v[60:61], v[34:35]
	v_mov_b64_e32 v[62:63], v[34:35]
	v_mov_b64_e32 v[64:65], v[34:35]
	v_mov_b64_e32 v[66:67], v[34:35]
	v_mov_b64_e32 v[68:69], v[34:35]
	v_mov_b64_e32 v[70:71], v[34:35]
	v_mov_b64_e32 v[72:73], v[34:35]
	v_mov_b64_e32 v[74:75], v[34:35]
	v_mov_b64_e32 v[76:77], v[34:35]
	v_mov_b64_e32 v[78:79], v[34:35]
	v_mov_b64_e32 v[80:81], v[34:35]
	v_mov_b64_e32 v[82:83], v[34:35]
	v_mov_b64_e32 v[84:85], v[34:35]
	v_mov_b64_e32 v[86:87], v[34:35]
	v_mov_b64_e32 v[88:89], v[34:35]
	v_mov_b64_e32 v[90:91], v[34:35]
	v_mov_b64_e32 v[92:93], v[34:35]
	v_mov_b64_e32 v[94:95], v[34:35]
	v_mov_b64_e32 v[96:97], v[34:35]
	v_mov_b64_e32 v[98:99], v[34:35]
	v_mov_b64_e32 v[100:101], v[34:35]
	v_mov_b64_e32 v[102:103], v[34:35]
	v_mov_b64_e32 v[104:105], v[34:35]
	v_mov_b64_e32 v[106:107], v[34:35]
	v_mov_b64_e32 v[108:109], v[34:35]
	v_mov_b64_e32 v[110:111], v[34:35]
	v_mov_b64_e32 v[112:113], v[34:35]
	v_mov_b64_e32 v[114:115], v[34:35]
	v_mov_b64_e32 v[116:117], v[34:35]
	v_mov_b64_e32 v[118:119], v[34:35]
	v_mov_b64_e32 v[120:121], v[34:35]
	v_mov_b64_e32 v[122:123], v[34:35]
	v_mov_b64_e32 v[124:125], v[34:35]
	v_mov_b64_e32 v[126:127], v[34:35]
	v_mov_b64_e32 v[128:129], v[34:35]
	v_mov_b64_e32 v[130:131], v[34:35]
	v_mov_b64_e32 v[132:133], v[34:35]
	v_mov_b64_e32 v[134:135], v[34:35]
	v_mov_b64_e32 v[136:137], v[34:35]
	v_mov_b64_e32 v[138:139], v[34:35]
	v_mov_b64_e32 v[140:141], v[34:35]
	v_mov_b64_e32 v[142:143], v[34:35]
	v_mov_b64_e32 v[144:145], v[34:35]
	v_mov_b64_e32 v[146:147], v[34:35]
	v_mov_b64_e32 v[148:149], v[34:35]
	v_mov_b64_e32 v[150:151], v[34:35]
	v_mov_b64_e32 v[152:153], v[34:35]
	v_mov_b64_e32 v[154:155], v[34:35]
	v_mov_b64_e32 v[156:157], v[34:35]
	v_mov_b64_e32 v[158:159], v[34:35]
	v_mov_b64_e32 v[160:161], v[34:35]

; #define PG8_SETVO(dst, u) do { _Pragma("unroll") for (int _h = 0; _h < 2; ++_h) _Pragma("unroll") for (int _i = 0; _i < 2; ++_i) { \
;         if constexpr (GATHER) { int R_, C_; stage_rc(tid * 16 + _i * 8192, R_, C_); dst[_h][_i] = (unsigned)(S.arow(u, R_ + HALF * _h) * K + C_) * 2u; } \
;         else dst[_h][_i] = voffA[_i] + (unsigned)_h * (unsigned)(HALF * K * 2); } } while (0)
; template <class Epi, class Sched, bool ALIGN_EPI = false, bool SP2 = false, bool F8 = false, bool GATHER = false>
; __device__ __forceinline__ void gemm_phase(PG8_LAS unsigned char* lds, const Gemm g, const Sched& S, const Epi& E) {
;     ...
;         const char* nA = (has_next && !GATHER) ? (const char*)g.A + (size_t)nxt.pm * tstep : cA; const char* nB = has_next ? (const char*)g.Bt + (size_t)nxt.pn * tstep : cB;
;         if (has_next) { PG8_SETVO(nvo, nxt); } else {
; #pragma unroll
;             for (int _h = 0; _h < 2; ++_h)
; #pragma unroll
;                 for (int _i = 0; _i < 2; ++_i) nvo[_h][_i] = vo[_h][_i]; }
;         for (int t = 0; t < nt; t += 2) {
;             const bool last = (t == nt - 2);
;             const char* a1 = cA + (size_t)(t + 1) * kstep;
;             const char* a2 = last ? nA : cA + (size_t)(t + 2) * kstep; const char* b2 = last ? nB : cB + (size_t)(t + 2) * kstep;
;             const char* a3 = a2 + kstep; const char* b3 = b2 + kstep;
;     ...
; #pragma unroll
;         for (int a = 0; a < 2; ++a)
; #pragma unroll
;             for (int b = 0; b < 2; ++b)
; #pragma unroll
;                 for (int m = 0; m < 4; ++m)
; #pragma unroll
;                     for (int n = 0; n < 2; ++n) acc[a][b][m][n] = (f32x4){0.f, 0.f, 0.f, 0.f};
.LBB0_995:
	s_ashr_i32 s70, s46, 4
	s_lshl_b32 s72, s46, 7
	s_ashr_i32 s71, s70, 31
	s_and_b32 s72, s72, 0x780
	s_lshl_b64 s[70:71], s[70:71], 13
	v_or_b32_e32 v2, s72, v195
	v_lshlrev_b32_e32 v2, 2, v2
	s_add_u32 s72, s16, s70
	s_addc_u32 s73, s17, s71
	global_load_dwordx4 v[240:243], v2, s[72:73]
	global_load_dwordx4 v[248:251], v2, s[72:73] offset:16
	s_add_u32 s70, s20, s70
	s_addc_u32 s71, s21, s71
	global_load_dwordx4 v[252:255], v2, s[70:71]
	global_load_dwordx2 v[244:245], v2, s[70:71] offset:16
	global_load_dword v247, v2, s[70:71] offset:24
	global_load_dword v190, v2, s[70:71] offset:28
	s_ashr_i32 s43, s42, 31
	s_lshl_b64 s[44:45], s[42:43], 19
	s_add_u32 s44, s2, s44
	s_addc_u32 s45, s3, s45
	s_and_b64 s[50:51], s[50:51], exec
	s_cselect_b32 s43, s45, s49
	s_cselect_b32 s63, s44, s48
	v_mov_b32_e32 v169, v163
	v_mov_b32_e32 v173, v163
	s_add_u32 s64, s48, 0x100
	v_mov_b32_e32 v34, 0
	v_lshl_add_u64 v[174:175], s[36:37], 0, v[172:173]
	v_lshl_add_u64 v[176:177], s[36:37], 0, v[168:169]
	s_addc_u32 s65, s49, 0
	s_mov_b32 s66, -2
	s_mov_b64 s[48:49], 0
	v_mov_b32_e32 v35, v34
	v_mov_b64_e32 v[36:37], v[34:35]
	v_mov_b64_e32 v[38:39], v[34:35]
	v_mov_b64_e32 v[40:41], v[34:35]
	v_mov_b64_e32 v[42:43], v[34:35]
	v_mov_b64_e32 v[44:45], v[34:35]
	v_mov_b64_e32 v[46:47], v[34:35]
	v_mov_b64_e32 v[48:49], v[34:35]
	v_mov_b64_e32 v[50:51], v[34:35]
	v_mov_b64_e32 v[52:53], v[34:35]
	v_mov_b64_e32 v[54:55], v[34:35]
	v_mov_b64_e32 v[56:57], v[34:35]
	v_mov_b64_e32 v[58:59], v[34:35]
	v_mov_b64_e32 v[60:61], v[34:35]
	v_mov_b64_e32 v[62:63], v[34:35]
	v_mov_b64_e32 v[64:65], v[34:35]
	v_mov_b64_e32 v[66:67], v[34:35]
	v_mov_b64_e32 v[68:69], v[34:35]
	v_mov_b64_e32 v[70:71], v[34:35]
	v_mov_b64_e32 v[72:73], v[34:35]
	v_mov_b64_e32 v[74:75], v[34:35]
	v_mov_b64_e32 v[76:77], v[34:35]
	v_mov_b64_e32 v[78:79], v[34:35]
	v_mov_b64_e32 v[80:81], v[34:35]
	v_mov_b64_e32 v[82:83], v[34:35]
	v_mov_b64_e32 v[84:85], v[34:35]
	v_mov_b64_e32 v[86:87], v[34:35]
	v_mov_b64_e32 v[88:89], v[34:35]
	v_mov_b64_e32 v[90:91], v[34:35]
	v_mov_b64_e32 v[92:93], v[34:35]
	v_mov_b64_e32 v[94:95], v[34:35]
	v_mov_b64_e32 v[96:97], v[34:35]
	v_mov_b64_e32 v[98:99], v[34:35]
	v_mov_b64_e32 v[100:101], v[34:35]
	v_mov_b64_e32 v[102:103], v[34:35]
	v_mov_b64_e32 v[104:105], v[34:35]
	v_mov_b64_e32 v[106:107], v[34:35]
	v_mov_b64_e32 v[108:109], v[34:35]
	v_mov_b64_e32 v[110:111], v[34:35]
	v_mov_b64_e32 v[112:113], v[34:35]
	v_mov_b64_e32 v[114:115], v[34:35]
	v_mov_b64_e32 v[116:117], v[34:35]
	v_mov_b64_e32 v[118:119], v[34:35]
	v_mov_b64_e32 v[120:121], v[34:35]
	v_mov_b64_e32 v[122:123], v[34:35]
	v_mov_b64_e32 v[124:125], v[34:35]
	v_mov_b64_e32 v[126:127], v[34:35]
	v_mov_b64_e32 v[128:129], v[34:35]
	v_mov_b64_e32 v[130:131], v[34:35]
	v_mov_b64_e32 v[132:133], v[34:35]
	v_mov_b64_e32 v[134:135], v[34:35]
	v_mov_b64_e32 v[136:137], v[34:35]
	v_mov_b64_e32 v[138:139], v[34:35]
	v_mov_b64_e32 v[140:141], v[34:35]
	v_mov_b64_e32 v[142:143], v[34:35]
	v_mov_b64_e32 v[144:145], v[34:35]
	v_mov_b64_e32 v[146:147], v[34:35]
	v_mov_b64_e32 v[148:149], v[34:35]
	v_mov_b64_e32 v[150:151], v[34:35]
	v_mov_b64_e32 v[152:153], v[34:35]
	v_mov_b64_e32 v[154:155], v[34:35]
	v_mov_b64_e32 v[156:157], v[34:35]
	v_mov_b64_e32 v[158:159], v[34:35]
	v_mov_b64_e32 v[160:161], v[34:35]

; #define PG8_SETVO(dst, u) do { _Pragma("unroll") for (int _h = 0; _h < 2; ++_h) _Pragma("unroll") for (int _i = 0; _i < 2; ++_i) { \
;         if constexpr (GATHER) { int R_, C_; stage_rc(tid * 16 + _i * 8192, R_, C_); dst[_h][_i] = (unsigned)(S.arow(u, R_ + HALF * _h) * K + C_) * 2u; } \
;         else dst[_h][_i] = voffA[_i] + (unsigned)_h * (unsigned)(HALF * K * 2); } } while (0)
; template <class Epi, class Sched, bool ALIGN_EPI = false, bool SP2 = false, bool F8 = false, bool GATHER = false>
; __device__ __forceinline__ void gemm_phase(PG8_LAS unsigned char* lds, const Gemm g, const Sched& S, const Epi& E) {
;     ...
;         const char* nA = (has_next && !GATHER) ? (const char*)g.A + (size_t)nxt.pm * tstep : cA; const char* nB = has_next ? (const char*)g.Bt + (size_t)nxt.pn * tstep : cB;
;         if (has_next) { PG8_SETVO(nvo, nxt); } else {
; #pragma unroll
;             for (int _h = 0; _h < 2; ++_h)
; #pragma unroll
;                 for (int _i = 0; _i < 2; ++_i) nvo[_h][_i] = vo[_h][_i]; }
;         for (int t = 0; t < nt; t += 2) {
;             const bool last = (t == nt - 2);
;             const char* a1 = cA + (size_t)(t + 1) * kstep;
;             const char* a2 = last ? nA : cA + (size_t)(t + 2) * kstep; const char* b2 = last ? nB : cB + (size_t)(t + 2) * kstep;
;             const char* a3 = a2 + kstep; const char* b3 = b2 + kstep;
;     ...
; #pragma unroll
;         for (int a = 0; a < 2; ++a)
; #pragma unroll
;             for (int b = 0; b < 2; ++b)
; #pragma unroll
;                 for (int m = 0; m < 4; ++m)
; #pragma unroll
;                     for (int n = 0; n < 2; ++n) acc[a][b][m][n] = (f32x4){0.f, 0.f, 0.f, 0.f};
.LBB0_1072:
	s_ashr_i32 s49, s48, 31
	s_lshl_b64 s[50:51], s[48:49], 19
	s_add_u32 s50, s9, s50
	s_addc_u32 s51, s10, s51
	s_and_b64 s[54:55], s[54:55], exec
	s_cselect_b32 s49, s51, s5
	s_cselect_b32 s68, s50, s4
	v_mov_b32_e32 v171, v167
	v_mov_b32_e32 v173, v167
	s_add_u32 s69, s4, 0x100
	v_mov_b32_e32 v34, 0
	v_lshl_add_u64 v[174:175], s[18:19], 0, v[172:173]
	v_lshl_add_u64 v[176:177], s[18:19], 0, v[170:171]
	s_addc_u32 s70, s5, 0
	s_mov_b32 s71, -2
	s_mov_b64 s[4:5], 0
	v_mov_b32_e32 v35, v34
	v_mov_b64_e32 v[36:37], v[34:35]
	v_mov_b64_e32 v[38:39], v[34:35]
	v_mov_b64_e32 v[40:41], v[34:35]
	v_mov_b64_e32 v[42:43], v[34:35]
	v_mov_b64_e32 v[44:45], v[34:35]
	v_mov_b64_e32 v[46:47], v[34:35]
	v_mov_b64_e32 v[48:49], v[34:35]
	v_mov_b64_e32 v[50:51], v[34:35]
	v_mov_b64_e32 v[52:53], v[34:35]
	v_mov_b64_e32 v[54:55], v[34:35]
	v_mov_b64_e32 v[56:57], v[34:35]
	v_mov_b64_e32 v[58:59], v[34:35]
	v_mov_b64_e32 v[60:61], v[34:35]
	v_mov_b64_e32 v[62:63], v[34:35]
	v_mov_b64_e32 v[64:65], v[34:35]
	v_mov_b64_e32 v[66:67], v[34:35]
	v_mov_b64_e32 v[68:69], v[34:35]
	v_mov_b64_e32 v[70:71], v[34:35]
	v_mov_b64_e32 v[72:73], v[34:35]
	v_mov_b64_e32 v[74:75], v[34:35]
	v_mov_b64_e32 v[76:77], v[34:35]
	v_mov_b64_e32 v[78:79], v[34:35]
	v_mov_b64_e32 v[80:81], v[34:35]
	v_mov_b64_e32 v[82:83], v[34:35]
	v_mov_b64_e32 v[84:85], v[34:35]
	v_mov_b64_e32 v[86:87], v[34:35]
	v_mov_b64_e32 v[88:89], v[34:35]
	v_mov_b64_e32 v[90:91], v[34:35]
	v_mov_b64_e32 v[92:93], v[34:35]
	v_mov_b64_e32 v[94:95], v[34:35]
	v_mov_b64_e32 v[96:97], v[34:35]
	v_mov_b64_e32 v[98:99], v[34:35]
	v_mov_b64_e32 v[100:101], v[34:35]
	v_mov_b64_e32 v[102:103], v[34:35]
	v_mov_b64_e32 v[104:105], v[34:35]
	v_mov_b64_e32 v[106:107], v[34:35]
	v_mov_b64_e32 v[108:109], v[34:35]
	v_mov_b64_e32 v[110:111], v[34:35]
	v_mov_b64_e32 v[112:113], v[34:35]
	v_mov_b64_e32 v[114:115], v[34:35]
	v_mov_b64_e32 v[116:117], v[34:35]
	v_mov_b64_e32 v[118:119], v[34:35]
	v_mov_b64_e32 v[120:121], v[34:35]
	v_mov_b64_e32 v[122:123], v[34:35]
	v_mov_b64_e32 v[124:125], v[34:35]
	v_mov_b64_e32 v[126:127], v[34:35]
	v_mov_b64_e32 v[128:129], v[34:35]
	v_mov_b64_e32 v[130:131], v[34:35]
	v_mov_b64_e32 v[132:133], v[34:35]
	v_mov_b64_e32 v[134:135], v[34:35]
	v_mov_b64_e32 v[136:137], v[34:35]
	v_mov_b64_e32 v[138:139], v[34:35]
	v_mov_b64_e32 v[140:141], v[34:35]
	v_mov_b64_e32 v[142:143], v[34:35]
	v_mov_b64_e32 v[144:145], v[34:35]
	v_mov_b64_e32 v[146:147], v[34:35]
	v_mov_b64_e32 v[148:149], v[34:35]
	v_mov_b64_e32 v[150:151], v[34:35]
	v_mov_b64_e32 v[152:153], v[34:35]
	v_mov_b64_e32 v[154:155], v[34:35]
	v_mov_b64_e32 v[156:157], v[34:35]
	v_mov_b64_e32 v[158:159], v[34:35]
	v_mov_b64_e32 v[160:161], v[34:35]
